# gemm_qkv: bias fragment prefetched before the K loop (was a serialized global load in the epilogue)
# speedup vs baseline: 1.0315x; 1.0063x over previous
_ZN4g2568gemm_qkvEPKDF16_S1_PKfPDF16_:
	s_load_dwordx8 s[4:11], s[0:1], 0x0
	s_lshl_b32 s0, s2, 1
	s_and_b32 s0, s0, 8
	s_lshr_b32 s1, s2, 5
	s_add_i32 s0, s0, s1
	s_lshl_b32 s1, s2, 2
	v_readfirstlane_b32 s26, v0
	s_bfe_u32 s3, s2, 0x20003
	s_and_b32 s1, s1, 12
	s_lshr_b32 s18, s26, 6
	s_lshl_b32 s0, s0, 8
	v_lshlrev_b32_e32 v1, 4, v0
	s_movk_i32 s12, 0x70
	s_or_b32 s24, s1, s3
	s_mov_b32 s1, 0
	v_bitop3_b32 v3, v1, s12, v0 bitop3:0x48
	v_lshlrev_b32_e32 v1, 8, v0
	s_mov_b32 s12, 0x3f800
	v_mov_b32_e32 v2, 0x20000
	s_lshr_b32 s25, s26, 8
	s_lshl_b32 s40, s18, 10
	s_lshl_b64 s[22:23], s[0:1], 11
	s_mul_i32 s1, s24, 0x60000
	v_bitop3_b32 v13, v1, s12, v2 bitop3:0xc8
	s_waitcnt lgkmcnt(0)
	v_bfe_u32 v190, v0, 4, 2
	s_and_b32 s44, s18, 3
	v_lshlrev_b32_e32 v190, 2, v190
	s_mul_i32 s45, s24, 0xc0
	v_lshl_or_b32 v191, s44, 5, v190
	v_add_u32_e32 v191, s45, v191
	v_lshlrev_b32_e32 v191, 2, v191
	v_lshl_or_b32 v192, s44, 4, v190
	v_or_b32_e32 v192, s45, v192
	v_lshlrev_b32_e32 v192, 2, v192
	global_load_dwordx4 v[194:197], v191, s[8:9]
	global_load_dwordx4 v[198:201], v191, s[8:9] offset:64
	global_load_dwordx4 v[202:205], v192, s[8:9] offset:512
	s_add_u32 s12, s6, s1
	v_and_b32_e32 v12, 0x1f800, v1
	s_addc_u32 s13, s7, 0
	s_add_i32 s27, s40, 0
	v_or_b32_e32 v98, v12, v3
	s_add_i32 m0, s27, 0x10000
	v_mov_b32_e32 v2, 0
	v_mov_b32_e32 v99, v2
	global_load_lds_dwordx4 v98, s[12:13]
	s_add_i32 m0, s27, 0x12000
	v_or_b32_e32 v100, v13, v3
	v_lshl_add_u64 v[4:5], s[12:13], 0, v[98:99]
	s_add_u32 s14, s4, s22
	s_mov_b64 s[16:17], 0x40000
	global_load_lds_dwordx4 v100, s[12:13]
	s_addc_u32 s15, s5, s23
	v_lshl_add_u64 v[6:7], v[4:5], 0, s[16:17]
	s_add_i32 m0, s27, 0x18000
	s_add_i32 s28, s27, 0x2000
	global_load_lds_dwordx4 v[6:7], off
	s_mov_b32 m0, s27
	s_add_u32 s20, s14, 0x40000
	global_load_lds_dwordx4 v98, s[14:15]
	s_mov_b32 m0, s28
	s_addc_u32 s21, s15, 0
	s_add_i32 s29, s27, 0x4000
	global_load_lds_dwordx4 v100, s[14:15]
	s_mov_b32 m0, s29
	s_add_i32 s30, s27, 0x6000
	global_load_lds_dwordx4 v98, s[20:21]
	s_mov_b32 m0, s30
	v_mov_b32_e32 v101, v2
	global_load_lds_dwordx4 v100, s[20:21]
	v_lshl_add_u64 v[10:11], s[12:13], 0, v[100:101]
	v_lshl_add_u64 v[8:9], s[14:15], 0, v[98:99]
	s_cmp_lg_u32 s25, 1
	v_lshl_add_u64 v[6:7], s[14:15], 0, v[100:101]
	s_cbranch_scc1 .LBB2_2
	s_barrier

.LBB2_6:
	v_lshlrev_b32_e32 v106, 2, v106
	s_mul_i32 s2, s24, 0xc0
	v_lshl_or_b32 v107, s1, 5, v106
	v_add_u32_e32 v108, s2, v107
	v_lshlrev_b32_e32 v109, 2, v108
	s_barrier
	v_mov_b32_e32 v98, v194
	v_mov_b32_e32 v99, v195
	v_mov_b32_e32 v100, v196
	v_mov_b32_e32 v101, v197
	v_mov_b32_e32 v102, v198
	v_mov_b32_e32 v103, v199
	v_mov_b32_e32 v104, v200
	v_mov_b32_e32 v105, v201
	v_lshl_or_b32 v1, s25, 6, v1
	s_movk_i32 s4, 0x190
	v_mul_lo_u32 v1, v1, s4
	v_lshl_or_b32 v113, s1, 4, v106
	s_movk_i32 s3, 0x400
	v_lshl_add_u32 v106, v107, 1, 0
	v_add_u32_e32 v114, 0x11300, v1
	v_or_b32_e32 v107, 16, v107
	v_or_b32_e32 v109, s2, v113
	v_mov_b32_e32 v111, 0x3e38aa3b
	v_cmp_gt_u32_e32 vcc, s3, v108
	v_add_u32_e32 v115, v106, v1
	v_add_u32_e32 v116, v106, v114
	v_add_u32_e32 v106, s2, v107
	v_lshl_add_u32 v117, v107, 1, 0
	v_lshlrev_b32_e32 v107, 2, v109
	v_cndmask_b32_e32 v110, 1.0, v111, vcc
	v_cmp_gt_u32_e32 vcc, s3, v106
	v_mov_b32_e32 v106, v202
	v_mov_b32_e32 v107, v203
	v_mov_b32_e32 v108, v204
	v_mov_b32_e32 v109, v205
	s_lshr_b32 s6, s0, 1
	v_cndmask_b32_e32 v112, 1.0, v111, vcc
	s_mul_i32 s7, s24, 3
	s_movk_i32 s0, 0x7e0
	s_cmp_gt_u32 s24, 5
	s_mul_i32 s8, s24, 0x1800
	s_waitcnt vmcnt(0)
	v_pk_add_f32 v[96:97], v[100:101], v[96:97]
	v_pk_add_f32 v[94:95], v[98:99], v[94:95]
	v_pk_add_f32 v[4:5], v[104:105], v[4:5]
	v_pk_add_f32 v[2:3], v[102:103], v[2:3]
	v_pk_add_f32 v[92:93], v[100:101], v[92:93]
	v_pk_add_f32 v[90:91], v[98:99], v[90:91]
	v_pk_add_f32 v[84:85], v[100:101], v[84:85]
	v_pk_add_f32 v[82:83], v[98:99], v[82:83]
	v_pk_add_f32 v[80:81], v[100:101], v[80:81]
	v_pk_add_f32 v[78:79], v[98:99], v[78:79]
	v_pk_add_f32 v[76:77], v[100:101], v[76:77]
	v_pk_add_f32 v[74:75], v[98:99], v[74:75]
	v_pk_add_f32 v[72:73], v[100:101], v[72:73]
	v_pk_add_f32 v[70:71], v[98:99], v[70:71]
	v_pk_add_f32 v[68:69], v[100:101], v[68:69]
	v_pk_add_f32 v[66:67], v[98:99], v[66:67]
	v_pk_add_f32 v[64:65], v[100:101], v[64:65]
	v_pk_add_f32 v[62:63], v[98:99], v[62:63]
	v_pk_mul_f32 v[96:97], v[110:111], v[96:97] op_sel_hi:[0,1]
	v_pk_mul_f32 v[94:95], v[110:111], v[94:95] op_sel_hi:[0,1]
	v_pk_mul_f32 v[4:5], v[112:113], v[4:5] op_sel_hi:[0,1]
	v_pk_mul_f32 v[2:3], v[112:113], v[2:3] op_sel_hi:[0,1]
	v_pk_mul_f32 v[92:93], v[110:111], v[92:93] op_sel_hi:[0,1]
	v_pk_mul_f32 v[90:91], v[110:111], v[90:91] op_sel_hi:[0,1]
	v_pk_mul_f32 v[84:85], v[110:111], v[84:85] op_sel_hi:[0,1]
	v_pk_mul_f32 v[82:83], v[110:111], v[82:83] op_sel_hi:[0,1]
	v_pk_mul_f32 v[80:81], v[110:111], v[80:81] op_sel_hi:[0,1]
	v_pk_mul_f32 v[78:79], v[110:111], v[78:79] op_sel_hi:[0,1]
	v_pk_mul_f32 v[76:77], v[110:111], v[76:77] op_sel_hi:[0,1]
	v_pk_mul_f32 v[74:75], v[110:111], v[74:75] op_sel_hi:[0,1]
	v_pk_mul_f32 v[72:73], v[110:111], v[72:73] op_sel_hi:[0,1]
	v_pk_mul_f32 v[70:71], v[110:111], v[70:71] op_sel_hi:[0,1]
	v_pk_mul_f32 v[68:69], v[110:111], v[68:69] op_sel_hi:[0,1]
	v_pk_mul_f32 v[66:67], v[110:111], v[66:67] op_sel_hi:[0,1]
	v_pk_mul_f32 v[64:65], v[110:111], v[64:65] op_sel_hi:[0,1]
	v_pk_mul_f32 v[62:63], v[110:111], v[62:63] op_sel_hi:[0,1]
	v_cvt_pk_f16_f32 v94, v94, v95
	v_cvt_pk_f16_f32 v95, v96, v97
	v_cvt_pk_f16_f32 v2, v2, v3
	v_cvt_pk_f16_f32 v3, v4, v5
	v_add_u32_e32 v4, v117, v114
	v_cvt_pk_f16_f32 v90, v90, v91
	v_cvt_pk_f16_f32 v91, v92, v93
	v_cvt_pk_f16_f32 v82, v82, v83
	v_cvt_pk_f16_f32 v83, v84, v85
	v_cvt_pk_f16_f32 v78, v78, v79
	v_cvt_pk_f16_f32 v79, v80, v81
	v_cvt_pk_f16_f32 v74, v74, v75
	v_cvt_pk_f16_f32 v75, v76, v77
	v_cvt_pk_f16_f32 v70, v70, v71
	v_cvt_pk_f16_f32 v71, v72, v73
	v_cvt_pk_f16_f32 v66, v66, v67
	v_cvt_pk_f16_f32 v67, v68, v69
	v_cvt_pk_f16_f32 v62, v62, v63
	v_cvt_pk_f16_f32 v63, v64, v65
	ds_write_b64 v115, v[94:95]
	ds_write_b64 v115, v[90:91] offset:6400
	ds_write_b64 v115, v[82:83] offset:12800
	ds_write_b64 v115, v[78:79] offset:19200
	ds_write_b64 v115, v[74:75] offset:51200
	ds_write_b64 v115, v[70:71] offset:57600
	ds_write_b64 v115, v[66:67] offset:64000
	ds_write_b64 v116, v[62:63]
	v_pk_add_f32 v[24:25], v[104:105], v[24:25]
	v_pk_add_f32 v[22:23], v[102:103], v[22:23]
	ds_write_b64 v4, v[2:3]
	v_or_b32_e32 v3, 0x80, v113
	v_pk_mul_f32 v[24:25], v[112:113], v[24:25] op_sel_hi:[0,1]
	v_pk_mul_f32 v[22:23], v[112:113], v[22:23] op_sel_hi:[0,1]
	v_add_u32_e32 v2, s2, v3
	v_add_u32_e32 v64, v117, v1
	v_cvt_pk_f16_f32 v22, v22, v23
	v_cvt_pk_f16_f32 v23, v24, v25
	v_cmp_gt_u32_e32 vcc, s3, v2
	ds_write_b64 v64, v[22:23] offset:64000
	v_pk_add_f32 v[4:5], v[108:109], v[56:57]
	v_cndmask_b32_e32 v2, 1.0, v111, vcc
	v_pk_add_f32 v[22:23], v[106:107], v[54:55]
	v_lshl_add_u32 v24, v3, 1, 0
	v_pk_mul_f32 v[4:5], v[2:3], v[4:5] op_sel_hi:[0,1]
	v_pk_mul_f32 v[22:23], v[2:3], v[22:23] op_sel_hi:[0,1]
	v_cvt_pk_f16_f32 v22, v22, v23
	v_cvt_pk_f16_f32 v23, v4, v5
	v_add_u32_e32 v1, v24, v1
	ds_write_b64 v1, v[22:23]
	v_pk_add_f32 v[4:5], v[108:109], v[44:45]
	v_pk_add_f32 v[22:23], v[106:107], v[42:43]
	v_pk_mul_f32 v[4:5], v[2:3], v[4:5] op_sel_hi:[0,1]
	v_pk_mul_f32 v[22:23], v[2:3], v[22:23] op_sel_hi:[0,1]
	v_cvt_pk_f16_f32 v22, v22, v23
	v_cvt_pk_f16_f32 v23, v4, v5
	ds_write_b64 v1, v[22:23] offset:6400
	v_pk_add_f32 v[4:5], v[108:109], v[36:37]
	v_pk_add_f32 v[22:23], v[106:107], v[34:35]
	v_pk_mul_f32 v[4:5], v[2:3], v[4:5] op_sel_hi:[0,1]
	v_pk_mul_f32 v[22:23], v[2:3], v[22:23] op_sel_hi:[0,1]
	v_cvt_pk_f16_f32 v22, v22, v23
	v_cvt_pk_f16_f32 v23, v4, v5
	ds_write_b64 v1, v[22:23] offset:12800
	v_pk_add_f32 v[4:5], v[108:109], v[28:29]
	v_pk_add_f32 v[22:23], v[106:107], v[26:27]
	v_pk_mul_f32 v[4:5], v[2:3], v[4:5] op_sel_hi:[0,1]
	v_pk_mul_f32 v[22:23], v[2:3], v[22:23] op_sel_hi:[0,1]
	v_cvt_pk_f16_f32 v22, v22, v23
	v_cvt_pk_f16_f32 v23, v4, v5
	v_pk_add_f32 v[4:5], v[108:109], v[20:21]
	v_pk_add_f32 v[18:19], v[106:107], v[18:19]
	v_pk_mul_f32 v[4:5], v[2:3], v[4:5] op_sel_hi:[0,1]
	v_pk_mul_f32 v[18:19], v[2:3], v[18:19] op_sel_hi:[0,1]
	v_cvt_pk_f16_f32 v18, v18, v19
	v_cvt_pk_f16_f32 v19, v4, v5
	v_pk_add_f32 v[4:5], v[108:109], v[16:17]
	v_pk_add_f32 v[14:15], v[106:107], v[14:15]
	v_pk_mul_f32 v[4:5], v[2:3], v[4:5] op_sel_hi:[0,1]
	v_pk_mul_f32 v[14:15], v[2:3], v[14:15] op_sel_hi:[0,1]
	v_cvt_pk_f16_f32 v14, v14, v15
	v_cvt_pk_f16_f32 v15, v4, v5
	v_pk_add_f32 v[4:5], v[108:109], v[12:13]
	v_pk_add_f32 v[10:11], v[106:107], v[10:11]
	v_pk_mul_f32 v[4:5], v[2:3], v[4:5] op_sel_hi:[0,1]
	v_pk_mul_f32 v[10:11], v[2:3], v[10:11] op_sel_hi:[0,1]
	v_cvt_pk_f16_f32 v10, v10, v11
	v_cvt_pk_f16_f32 v11, v4, v5
	v_pk_add_f32 v[4:5], v[108:109], v[8:9]
	v_pk_add_f32 v[6:7], v[106:107], v[6:7]
	v_pk_mul_f32 v[4:5], v[2:3], v[4:5] op_sel_hi:[0,1]
	v_pk_mul_f32 v[2:3], v[2:3], v[6:7] op_sel_hi:[0,1]
	v_pk_add_f32 v[88:89], v[104:105], v[88:89]
	v_pk_add_f32 v[86:87], v[102:103], v[86:87]
	v_pk_add_f32 v[60:61], v[104:105], v[60:61]
	v_pk_add_f32 v[58:59], v[102:103], v[58:59]
	v_pk_add_f32 v[52:53], v[104:105], v[52:53]
	v_pk_add_f32 v[50:51], v[102:103], v[50:51]
	v_pk_add_f32 v[48:49], v[104:105], v[48:49]
	v_pk_add_f32 v[46:47], v[102:103], v[46:47]
	v_pk_add_f32 v[40:41], v[104:105], v[40:41]
	v_pk_add_f32 v[38:39], v[102:103], v[38:39]
	v_pk_add_f32 v[32:33], v[104:105], v[32:33]
	v_pk_add_f32 v[30:31], v[102:103], v[30:31]
	ds_write_b64 v1, v[22:23] offset:19200
	ds_write_b64 v1, v[18:19] offset:51200
	ds_write_b64 v1, v[14:15] offset:57600
	ds_write_b64 v1, v[10:11] offset:64000
	v_cvt_pk_f16_f32 v2, v2, v3
	v_cvt_pk_f16_f32 v3, v4, v5
	v_add_u32_e32 v1, v24, v114
	v_lshrrev_b32_e32 v10, 2, v0
	v_pk_mul_f32 v[88:89], v[112:113], v[88:89] op_sel_hi:[0,1]
	v_pk_mul_f32 v[86:87], v[112:113], v[86:87] op_sel_hi:[0,1]
	v_pk_mul_f32 v[60:61], v[112:113], v[60:61] op_sel_hi:[0,1]
	v_pk_mul_f32 v[58:59], v[112:113], v[58:59] op_sel_hi:[0,1]
	v_pk_mul_f32 v[52:53], v[112:113], v[52:53] op_sel_hi:[0,1]
	v_pk_mul_f32 v[50:51], v[112:113], v[50:51] op_sel_hi:[0,1]
	v_pk_mul_f32 v[48:49], v[112:113], v[48:49] op_sel_hi:[0,1]
	v_pk_mul_f32 v[46:47], v[112:113], v[46:47] op_sel_hi:[0,1]
	v_pk_mul_f32 v[40:41], v[112:113], v[40:41] op_sel_hi:[0,1]
	v_pk_mul_f32 v[38:39], v[112:113], v[38:39] op_sel_hi:[0,1]
	v_pk_mul_f32 v[32:33], v[112:113], v[32:33] op_sel_hi:[0,1]
	v_pk_mul_f32 v[30:31], v[112:113], v[30:31] op_sel_hi:[0,1]
	ds_write_b64 v1, v[2:3]
	v_and_b32_e32 v13, 3, v0
	v_or_b32_e32 v1, s6, v10
	v_cvt_pk_f16_f32 v62, v86, v87
	v_cvt_pk_f16_f32 v63, v88, v89
	v_cvt_pk_f16_f32 v58, v58, v59
	v_cvt_pk_f16_f32 v59, v60, v61
	v_cvt_pk_f16_f32 v50, v50, v51
	v_cvt_pk_f16_f32 v51, v52, v53
	v_cvt_pk_f16_f32 v46, v46, v47
	v_cvt_pk_f16_f32 v47, v48, v49
	v_cvt_pk_f16_f32 v38, v38, v39
	v_cvt_pk_f16_f32 v39, v40, v41
	v_cvt_pk_f16_f32 v30, v30, v31
	v_cvt_pk_f16_f32 v31, v32, v33
	v_lshrrev_b32_e32 v17, 6, v1
	v_lshlrev_b32_e32 v1, 3, v13
	v_lshlrev_b32_e32 v2, 3, v0
	ds_write_b64 v64, v[62:63]
	ds_write_b64 v64, v[58:59] offset:6400
	ds_write_b64 v64, v[50:51] offset:12800
	ds_write_b64 v64, v[46:47] offset:19200
	ds_write_b64 v64, v[38:39] offset:51200
	ds_write_b64 v64, v[30:31] offset:57600
	v_and_or_b32 v1, v2, s0, v1
	v_and_b32_e32 v11, 0x7f, v0
	s_cselect_b64 s[0:1], -1, 0
	s_and_b32 s2, s7, 48
	s_waitcnt lgkmcnt(0)
	s_barrier
	v_or_b32_e32 v3, s6, v11
	s_cmp_lg_u32 s2, 16
	s_mul_i32 s2, s24, 0x60
	v_lshrrev_b32_e32 v18, 6, v3
	v_and_b32_e32 v8, 7, v0
	s_cselect_b64 s[4:5], -1, 0
	s_and_b32 s2, s2, 0x1e0
	v_and_b32_e32 v12, 0x1f8, v2
	v_lshlrev_b32_e32 v9, 3, v8
	v_add_u32_e32 v4, s2, v17
	v_add_u32_e32 v2, s2, v18
	s_and_b64 vcc, exec, s[0:1]
	s_cbranch_vccz .LBB2_9
	s_and_b64 vcc, exec, s[4:5]
	s_cbranch_vccz .LBB2_10
	v_mov_b32_e32 v5, 0
	v_lshlrev_b64 v[6:7], 12, v[4:5]
	v_or_b32_e32 v6, v6, v1
	s_mov_b64 s[2:3], 0x800000
	v_lshl_add_u64 v[6:7], v[6:7], 0, s[2:3]
	v_mov_b32_e32 v5, v13
	v_mov_b32_e32 v3, v10
	s_cbranch_execz .LBB2_11
	s_branch .LBB2_12

	.amdhsa_kernel _ZN4g2568gemm_qkvEPKDF16_S1_PKfPDF16_
		.amdhsa_group_segment_fixed_size 0
		.amdhsa_private_segment_fixed_size 0
		.amdhsa_kernarg_size 32
		.amdhsa_user_sgpr_count 2
		.amdhsa_user_sgpr_dispatch_ptr 0
		.amdhsa_user_sgpr_queue_ptr 0
		.amdhsa_user_sgpr_kernarg_segment_ptr 1
		.amdhsa_user_sgpr_dispatch_id 0
		.amdhsa_user_sgpr_kernarg_preload_length 0
		.amdhsa_user_sgpr_kernarg_preload_offset 0
		.amdhsa_user_sgpr_private_segment_size 0
		.amdhsa_uses_dynamic_stack 0
		.amdhsa_enable_private_segment 0
		.amdhsa_system_sgpr_workgroup_id_x 1
		.amdhsa_system_sgpr_workgroup_id_y 0
		.amdhsa_system_sgpr_workgroup_id_z 0
		.amdhsa_system_sgpr_workgroup_info 0
		.amdhsa_system_vgpr_workitem_id 0
		.amdhsa_next_free_vgpr 206
		.amdhsa_next_free_sgpr 46
		.amdhsa_accum_offset 208
		.amdhsa_reserve_vcc 1
		.amdhsa_float_round_mode_32 0
		.amdhsa_float_round_mode_16_64 0
		.amdhsa_float_denorm_mode_32 3
		.amdhsa_float_denorm_mode_16_64 3
		.amdhsa_dx10_clamp 1
		.amdhsa_ieee_mode 1
		.amdhsa_fp16_overflow 0
		.amdhsa_tg_split 0
		.amdhsa_exception_fp_ieee_invalid_op 0
		.amdhsa_exception_fp_denorm_src 0
		.amdhsa_exception_fp_ieee_div_zero 0
		.amdhsa_exception_fp_ieee_overflow 0
		.amdhsa_exception_fp_ieee_underflow 0
		.amdhsa_exception_fp_ieee_inexact 0
		.amdhsa_exception_int_div_zero 0
	.end_amdhsa_kernel

amdhsa.kernels:
  - .agpr_count:     0
    .args:
      - .actual_access:  read_only
        .address_space:  global
        .offset:         0
        .size:           8
        .value_kind:     global_buffer
      - .actual_access:  read_only
        .address_space:  global
        .offset:         8
        .size:           8
        .value_kind:     global_buffer
      - .actual_access:  read_only
        .address_space:  global
        .offset:         16
        .size:           8
        .value_kind:     global_buffer
      - .actual_access:  read_only
        .address_space:  global
        .offset:         24
        .size:           8
        .value_kind:     global_buffer
      - .actual_access:  read_only
        .address_space:  global
        .offset:         32
        .size:           8
        .value_kind:     global_buffer
      - .actual_access:  write_only
        .address_space:  global
        .offset:         40
        .size:           8
        .value_kind:     global_buffer
      - .actual_access:  read_only
        .address_space:  global
        .offset:         48
        .size:           8
        .value_kind:     global_buffer
      - .actual_access:  read_only
        .address_space:  global
        .offset:         56
        .size:           8
        .value_kind:     global_buffer
      - .actual_access:  read_only
        .address_space:  global
        .offset:         64
        .size:           8
        .value_kind:     global_buffer
      - .actual_access:  write_only
        .address_space:  global
        .offset:         72
        .size:           8
        .value_kind:     global_buffer
    .group_segment_fixed_size: 0
    .kernarg_segment_align: 8
    .kernarg_segment_size: 80
    .language:       OpenCL C
    .language_version:
      - 2
      - 0
    .max_flat_workgroup_size: 256
    .name:           _Z7cvt_allPKfS0_S0_S0_S0_PDF16_S0_S0_S0_Pf
    .private_segment_fixed_size: 0
    .sgpr_count:     16
    .sgpr_spill_count: 0
    .symbol:         _Z7cvt_allPKfS0_S0_S0_S0_PDF16_S0_S0_S0_Pf.kd
    .uniform_work_group_size: 1
    .uses_dynamic_stack: false
    .vgpr_count:     22
    .vgpr_spill_count: 0
    .wavefront_size: 64
  - .agpr_count:     0
    .args:
      - .address_space:  global
        .offset:         0
        .size:           8
        .value_kind:     global_buffer
      - .address_space:  global
        .offset:         8
        .size:           8
        .value_kind:     global_buffer
      - .actual_access:  read_only
        .address_space:  global
        .offset:         16
        .size:           8
        .value_kind:     global_buffer
      - .actual_access:  write_only
        .address_space:  global
        .offset:         24
        .size:           8
        .value_kind:     global_buffer
      - .offset:         32
        .size:           4
        .value_kind:     hidden_block_count_x
      - .offset:         36
        .size:           4
        .value_kind:     hidden_block_count_y
      - .offset:         40
        .size:           4
        .value_kind:     hidden_block_count_z
      - .offset:         44
        .size:           2
        .value_kind:     hidden_group_size_x
      - .offset:         46
        .size:           2
        .value_kind:     hidden_group_size_y
      - .offset:         48
        .size:           2
        .value_kind:     hidden_group_size_z
      - .offset:         50
        .size:           2
        .value_kind:     hidden_remainder_x
      - .offset:         52
        .size:           2
        .value_kind:     hidden_remainder_y
      - .offset:         54
        .size:           2
        .value_kind:     hidden_remainder_z
      - .offset:         72
        .size:           8
        .value_kind:     hidden_global_offset_x
      - .offset:         80
        .size:           8
        .value_kind:     hidden_global_offset_y
      - .offset:         88
        .size:           8
        .value_kind:     hidden_global_offset_z
      - .offset:         96
        .size:           2
        .value_kind:     hidden_grid_dims
      - .offset:         152
        .size:           4
        .value_kind:     hidden_dynamic_lds_size
    .group_segment_fixed_size: 0
    .kernarg_segment_align: 8
    .kernarg_segment_size: 288
    .language:       OpenCL C
    .language_version:
      - 2
      - 0
    .max_flat_workgroup_size: 512
    .name:           _ZN6g128w88gemm_outEPKDF16_S1_PKfPf
    .private_segment_fixed_size: 0
    .sgpr_count:     29
    .sgpr_spill_count: 0
    .symbol:         _ZN6g128w88gemm_outEPKDF16_S1_PKfPf.kd
    .uniform_work_group_size: 1
    .uses_dynamic_stack: false
    .vgpr_count:     116
    .vgpr_spill_count: 0
    .wavefront_size: 64
  - .agpr_count:     0
    .args:
      - .address_space:  global
        .offset:         0
        .size:           8
        .value_kind:     global_buffer
      - .address_space:  global
        .offset:         8
        .size:           8
        .value_kind:     global_buffer
      - .actual_access:  read_only
        .address_space:  global
        .offset:         16
        .size:           8
        .value_kind:     global_buffer
      - .actual_access:  write_only
        .address_space:  global
        .offset:         24
        .size:           8
        .value_kind:     global_buffer
    .group_segment_fixed_size: 0
    .kernarg_segment_align: 8
    .kernarg_segment_size: 32
    .language:       OpenCL C
    .language_version:
      - 2
      - 0
    .max_flat_workgroup_size: 512
    .name:           _ZN4g2568gemm_qkvEPKDF16_S1_PKfPDF16_
    .private_segment_fixed_size: 0
    .sgpr_count:     52
    .sgpr_spill_count: 0
    .symbol:         _ZN4g2568gemm_qkvEPKDF16_S1_PKfPDF16_.kd
    .uniform_work_group_size: 1
    .uses_dynamic_stack: false
    .vgpr_count:     206
    .vgpr_spill_count: 0
    .wavefront_size: 64
  - .agpr_count:     0
    .args:
      - .address_space:  global
        .offset:         0
        .size:           8
        .value_kind:     global_buffer
      - .actual_access:  write_only
        .address_space:  global
        .offset:         8
        .size:           8
        .value_kind:     global_buffer
    .group_segment_fixed_size: 0
    .kernarg_segment_align: 8
    .kernarg_segment_size: 16
    .language:       OpenCL C
    .language_version:
      - 2
      - 0
    .max_flat_workgroup_size: 512
    .name:           _ZN3att8attn_fwdEPKDF16_PDF16_
    .private_segment_fixed_size: 0
    .sgpr_count:     42
    .sgpr_spill_count: 0
    .symbol:         _ZN3att8attn_fwdEPKDF16_PDF16_.kd
    .uniform_work_group_size: 1
    .uses_dynamic_stack: false
    .vgpr_count:     204
    .vgpr_spill_count: 0
    .wavefront_size: 64
